# union 6: expert GEMM1 next-unit token-index loads into distinct registers, one wait instead of three
# speedup vs baseline: 1.0124x; 1.0072x over previous
.LBB0_1022:
	v_cndmask_b32_e64 v2, 0, 1, s[4:5]
	v_cmp_ne_u32_e64 s[0:1], 1, v2
	s_andn2_b64 vcc, exec, s[4:5]
	s_mov_b64 s[34:35], s[38:39]
	v_mov_b32_e32 v204, v178
	v_mov_b32_e32 v201, v174
	v_mov_b32_e32 v202, v176
	v_mov_b32_e32 v203, v173
	s_cbranch_vccnz .LBB0_1040
	s_lshl_b32 s4, s26, 2
	s_add_i32 s4, s4, 0
	s_add_i32 s4, s4, 0x20180
	v_mov_b32_e32 v2, s4
	ds_read_b32 v6, v2
	s_ashr_i32 s27, s26, 31
	s_cmp_lt_i32 s26, 64
	s_cselect_b64 s[34:35], -1, 0
	s_cmp_gt_i32 s26, 63
	v_add_u32_e32 v2, s30, v162
	v_mov_b32_e32 v244, v2
	s_cbranch_scc1 .LBB0_1027
	s_waitcnt lgkmcnt(0)
	v_cmp_lt_i32_e32 vcc, v2, v6
	v_mov_b32_e32 v244, 0
	s_and_saveexec_b64 s[4:5], vcc
	s_cbranch_execz .LBB0_1026
	s_lshl_b64 s[40:41], s[26:27], 15
	s_add_u32 s40, s42, s40
	s_addc_u32 s41, s43, s41
	v_ashrrev_i32_e32 v3, 31, v2
	v_lshl_add_u64 v[2:3], v[2:3], 2, s[40:41]
	global_load_dword v244, v[2:3], off

.LBB0_1027:
	v_cndmask_b32_e64 v3, 0, 1, s[34:35]
	v_cmp_ne_u32_e64 s[4:5], 1, v3
	s_andn2_b64 vcc, exec, s[34:35]
	v_add_u32_e32 v4, s30, v164
	v_mov_b32_e32 v245, v4
	s_cbranch_vccnz .LBB0_1032
	s_waitcnt lgkmcnt(0)
	v_cmp_lt_i32_e32 vcc, v4, v6
	v_mov_b32_e32 v245, 0
	s_and_saveexec_b64 s[34:35], vcc
	s_cbranch_execz .LBB0_1030
	s_lshl_b64 s[40:41], s[26:27], 15
	s_add_u32 s40, s42, s40
	s_addc_u32 s41, s43, s41
	v_ashrrev_i32_e32 v5, 31, v4
	v_lshl_add_u64 v[4:5], v[4:5], 2, s[40:41]
	global_load_dword v245, v[4:5], off
.LBB0_1030:
	s_or_b64 exec, exec, s[34:35]
	s_add_i32 s11, s30, 0x80
	s_and_b64 vcc, exec, s[4:5]
	v_add_u32_e32 v3, s11, v162
	s_cbranch_vccz .LBB0_1033

.LBB0_1039:
	s_lshl_b64 s[4:5], s[26:27], 21
	s_add_u32 s11, s15, s4
	s_addc_u32 s27, s44, s5
	s_ashr_i32 s29, s28, 31
	s_lshl_b64 s[4:5], s[28:29], 19
	s_add_u32 s34, s11, s4
	s_waitcnt vmcnt(0)
	v_lshl_or_b32 v201, v3, 11, v1
	v_lshl_or_b32 v202, v245, 11, v1
	v_lshl_or_b32 v203, v244, 11, v1
	s_addc_u32 s35, s27, s5
	v_lshl_or_b32 v204, v5, 11, v1
